# speedup vs baseline: 1.0800x; 1.0011x over previous
.LBB2_17:
	s_and_b64 vcc, exec, s[2:3]
	s_cbranch_vccz .LBB2_27
	s_setprio 1
	v_mov_b32_e32 v240, 0x64646464
	s_mov_b32 s42, 0x4010400
	s_mov_b32 s43, 0x4030402
	s_load_dwordx2 s[2:3], s[0:1], 0x70
	s_load_dwordx4 s[4:7], s[0:1], 0x40
	s_load_dwordx2 s[36:37], s[0:1], 0x60
	s_lshr_b32 s11, s15, 7
	s_lshl_b32 s8, s12, 3
	s_or_b32 s8, s11, s8
	s_ashr_i32 s9, s8, 31
	s_bfe_u32 s10, s15, 0x10006
	s_lshl_b64 s[12:13], s[8:9], 12
	v_and_b32_e32 v156, 63, v0
	s_waitcnt lgkmcnt(0)
	s_add_u32 s12, s2, s12
	s_addc_u32 s13, s3, s13
	v_lshlrev_b32_e32 v24, 2, v0
	v_and_b32_e32 v24, 0xfc, v24
	v_lshl_or_b32 v24, s14, 8, v24
	global_load_dword v27, v24, s[36:37]
	v_lshlrev_b32_e32 v1, 3, v156
	global_load_dwordx2 v[154:155], v1, s[12:13]
	global_load_dwordx2 v[150:151], v1, s[12:13] offset:512
	global_load_dwordx2 v[146:147], v1, s[12:13] offset:1024
	global_load_dwordx2 v[142:143], v1, s[12:13] offset:1536
	global_load_dwordx2 v[152:153], v1, s[12:13] offset:2048
	global_load_dwordx2 v[148:149], v1, s[12:13] offset:2560
	global_load_dwordx2 v[144:145], v1, s[12:13] offset:3072
	global_load_dwordx2 v[140:141], v1, s[12:13] offset:3584
	s_lshl_b32 s9, s14, 10
	s_lshl_b32 s12, s10, 9
	s_or_b32 s9, s12, s9
	v_or_b32_e32 v1, s9, v156
	v_lshlrev_b32_e32 v2, 4, v1
	v_mov_b32_e32 v3, 0
	v_lshl_add_u64 v[4:5], s[4:5], 0, v[2:3]
	s_movk_i32 s9, 0x1000
	v_add_co_u32_e32 v4, vcc, s9, v4
	v_lshlrev_b32_e32 v1, 2, v0
	s_nop 0
	v_addc_co_u32_e32 v5, vcc, 0, v5, vcc
	global_load_dwordx4 v[86:89], v[4:5], off
	global_load_dwordx4 v[78:81], v[4:5], off offset:1024
	global_load_dwordx4 v[70:73], v[4:5], off offset:2048
	global_load_dwordx4 v[66:69], v[4:5], off offset:3072
	global_load_dwordx4 v[122:125], v2, s[4:5]
	global_load_dwordx4 v[126:129], v2, s[6:7]
	global_load_dwordx4 v[114:117], v2, s[4:5] offset:1024
	global_load_dwordx4 v[118:121], v2, s[6:7] offset:1024
	global_load_dwordx4 v[106:109], v2, s[4:5] offset:2048
	global_load_dwordx4 v[110:113], v2, s[6:7] offset:2048
	global_load_dwordx4 v[98:101], v2, s[4:5] offset:3072
	global_load_dwordx4 v[102:105], v2, s[6:7] offset:3072
	v_lshl_add_u64 v[4:5], s[6:7], 0, v[2:3]
	v_add_co_u32_e32 v2, vcc, 0x1000, v4
	s_nop 1
	v_addc_co_u32_e32 v3, vcc, 0, v5, vcc
	global_load_dwordx4 v[94:97], v[2:3], off
	global_load_dwordx4 v[90:93], v[2:3], off offset:1024
	global_load_dwordx4 v[82:85], v[2:3], off offset:2048
	global_load_dwordx4 v[74:77], v[2:3], off offset:3072
	v_cmp_gt_u32_e32 vcc, 64, v0
	s_and_saveexec_b64 s[4:5], vcc
	s_cbranch_execz .LBB2_20
	v_add_u32_e32 v3, 0x1ee00, v1
	s_waitcnt vmcnt(24)
	ds_write_b32 v3, v27

.LBB3_17:
	s_and_b64 vcc, exec, s[2:3]
	s_cbranch_vccz .LBB3_27
	s_setprio 1
	v_mov_b32_e32 v240, 0x64646464
	s_mov_b32 s42, 0x4010400
	s_mov_b32 s43, 0x4030402
	s_load_dwordx2 s[8:9], s[0:1], 0x70
	s_load_dwordx4 s[4:7], s[0:1], 0x40
	s_load_dwordx4 s[20:23], s[0:1], 0x10
	s_load_dwordx4 s[28:31], s[0:1], 0x20
	s_load_dwordx4 s[32:35], s[0:1], 0x30
	s_load_dwordx2 s[36:37], s[0:1], 0x60
	v_mov_b32_e32 v3, 0
	v_lshlrev_b32_e32 v2, 2, v0
	s_movk_i32 s2, 0xfe00
	s_mov_b32 s3, -1
	s_waitcnt lgkmcnt(0)
	v_lshl_add_u64 v[6:7], s[22:23], 0, v[2:3]
	s_lshr_b32 s16, s15, 7
	s_movk_i32 s10, 0x80
	v_lshl_add_u64 v[6:7], v[6:7], 0, s[2:3]
	s_lshl_b32 s2, s12, 3
	v_cmp_gt_u32_e32 vcc, s10, v0
	s_or_b32 s10, s16, s2
	v_lshl_add_u64 v[4:5], s[20:21], 0, v[2:3]
	s_ashr_i32 s11, s10, 31
	v_cndmask_b32_e32 v6, v6, v4, vcc
	s_movk_i32 s17, 0x1000
	s_bfe_u32 s13, s15, 0x10006
	s_lshl_b64 s[2:3], s[10:11], 12
	v_and_b32_e32 v156, 63, v0
	v_cndmask_b32_e32 v7, v7, v5, vcc
	v_add_co_u32_e32 v20, vcc, s17, v6
	s_add_u32 s2, s8, s2
	s_nop 0
	v_addc_co_u32_e32 v21, vcc, 0, v7, vcc
	s_addc_u32 s3, s9, s3
	v_lshlrev_b32_e32 v1, 3, v156
	global_load_dword v17, v[6:7], off
	global_load_dword v16, v[6:7], off offset:512
	global_load_dword v13, v[6:7], off offset:1024
	global_load_dword v12, v[6:7], off offset:1536
	global_load_dword v9, v[6:7], off offset:2048
	global_load_dword v8, v[6:7], off offset:2560
	global_load_dword v5, v[6:7], off offset:3072
	global_load_dword v4, v[6:7], off offset:3584
	global_load_dword v19, v[20:21], off
	global_load_dword v18, v[20:21], off offset:512
	global_load_dword v15, v[20:21], off offset:1024
	global_load_dword v14, v[20:21], off offset:1536
	global_load_dword v11, v[20:21], off offset:2048
	global_load_dword v10, v[20:21], off offset:2560
	global_load_dword v7, v[20:21], off offset:3072
	global_load_dword v6, v[20:21], off offset:3584
	s_cmpk_lt_u32 s15, 0x80
	s_cselect_b32 s38, s28, s32
	s_cselect_b32 s39, s29, s33
	s_cselect_b32 s40, s30, s34
	s_cselect_b32 s41, s31, s35
	v_and_b32_e32 v24, 0x1fc, v2
	v_and_b32_e32 v28, 0xfc, v2
	v_lshl_or_b32 v28, s14, 8, v28
	global_load_dword v25, v24, s[38:39]
	global_load_dword v26, v24, s[40:41]
	global_load_dword v27, v28, s[36:37]
	global_load_dwordx2 v[154:155], v1, s[2:3]
	global_load_dwordx2 v[150:151], v1, s[2:3] offset:512
	global_load_dwordx2 v[146:147], v1, s[2:3] offset:1024
	global_load_dwordx2 v[142:143], v1, s[2:3] offset:1536
	global_load_dwordx2 v[152:153], v1, s[2:3] offset:2048
	global_load_dwordx2 v[148:149], v1, s[2:3] offset:2560
	global_load_dwordx2 v[144:145], v1, s[2:3] offset:3072
	global_load_dwordx2 v[140:141], v1, s[2:3] offset:3584
	s_lshl_b32 s2, s14, 10
	s_lshl_b32 s3, s13, 9
	s_or_b32 s2, s3, s2
	v_or_b32_e32 v1, s2, v156
	v_lshlrev_b32_e32 v20, 4, v1
	v_mov_b32_e32 v21, v3
	v_lshl_add_u64 v[22:23], s[4:5], 0, v[20:21]
	v_add_co_u32_e32 v22, vcc, s17, v22
	s_movk_i32 s2, 0x7f
	s_nop 0
	v_addc_co_u32_e32 v23, vcc, 0, v23, vcc
	global_load_dwordx4 v[86:89], v[22:23], off
	global_load_dwordx4 v[78:81], v[22:23], off offset:1024
	global_load_dwordx4 v[70:73], v[22:23], off offset:2048
	global_load_dwordx4 v[66:69], v[22:23], off offset:3072
	global_load_dwordx4 v[122:125], v20, s[4:5]
	global_load_dwordx4 v[126:129], v20, s[6:7]
	global_load_dwordx4 v[114:117], v20, s[4:5] offset:1024
	global_load_dwordx4 v[118:121], v20, s[6:7] offset:1024
	global_load_dwordx4 v[106:109], v20, s[4:5] offset:2048
	global_load_dwordx4 v[110:113], v20, s[6:7] offset:2048
	global_load_dwordx4 v[98:101], v20, s[4:5] offset:3072
	global_load_dwordx4 v[102:105], v20, s[6:7] offset:3072
	v_lshl_add_u64 v[22:23], s[6:7], 0, v[20:21]
	v_add_co_u32_e32 v20, vcc, 0x1000, v22
	s_nop 1
	v_addc_co_u32_e32 v21, vcc, 0, v23, vcc
	global_load_dwordx4 v[94:97], v[20:21], off
	global_load_dwordx4 v[90:93], v[20:21], off offset:1024
	global_load_dwordx4 v[82:85], v[20:21], off offset:2048
	global_load_dwordx4 v[74:77], v[20:21], off offset:3072
	v_cmp_lt_u32_e32 vcc, s2, v0
	v_cmp_gt_u32_e64 s[2:3], 64, v0
	s_and_saveexec_b64 s[4:5], s[2:3]
	s_cbranch_execz .LBB3_20
	v_add_u32_e32 v20, 0x1ee00, v2
	s_waitcnt vmcnt(24)
	ds_write_b32 v20, v27
